# attention loop: removed per-MFMA vmcnt waits made redundant by the K transposition wait, merged the per-row waits of the V staging writes; on top of v14
# baseline (speedup 1.0000x reference)
.LBB0_736:
	s_waitcnt vmcnt(24)
	ds_write_b128 v196, v[14:17]
	ds_write_b128 v197, v[18:21] offset:1024
	ds_write_b128 v196, v[22:25] offset:2048
	ds_write_b128 v197, v[26:29] offset:3072
	ds_read_b128 v[14:17], v198
	ds_read_b128 v[18:21], v199
	ds_read_b128 v[22:25], v198 offset:2048
	ds_read_b128 v[26:29], v199 offset:2048
	ds_write_b128 v196, v[30:33]
	ds_write_b128 v197, v[34:37] offset:1024
	ds_write_b128 v196, v[38:41] offset:2048
	ds_write_b128 v197, v[42:45] offset:3072
	ds_read_b128 v[30:33], v198
	ds_read_b128 v[34:37], v199
	ds_read_b128 v[38:41], v198 offset:2048
	ds_read_b128 v[42:45], v199 offset:2048
	s_waitcnt lgkmcnt(0)
	v_mfma_f32_16x16x32_bf16 v[170:173], v[14:17], v[6:9], v[170:173]
	s_mov_b32 s12, 0x40c00000
	v_mfma_f32_16x16x32_bf16 v[182:185], v[18:21], v[10:13], v[170:173]
	v_mfma_f32_16x16x32_bf16 v[170:173], v[22:25], v[6:9], v[174:177]
	v_mfma_f32_16x16x32_bf16 v[178:181], v[26:29], v[10:13], v[170:173]
	s_nop 3
	v_max_f32_e32 v0, v185, v185
	v_max_f32_e32 v153, v184, v184
	v_max_f32_e32 v0, v153, v0
	v_mfma_f32_16x16x32_bf16 v[170:173], v[30:33], v[6:9], v[186:189]
	v_max3_f32 v0, v182, v183, v0
	v_max_f32_e32 v153, v181, v181
	v_mfma_f32_16x16x32_bf16 v[174:177], v[34:37], v[10:13], v[170:173]
	v_max_f32_e32 v186, v180, v180
	v_max_f32_e32 v153, v186, v153
	v_max3_f32 v153, v178, v179, v153
	s_waitcnt lgkmcnt(0)
	v_mfma_f32_16x16x32_bf16 v[170:173], v[38:41], v[6:9], v[190:193]
	v_mfma_f32_16x16x32_bf16 v[170:173], v[42:45], v[10:13], v[170:173]
	s_nop 0
	v_max_f32_e32 v186, v175, v175
	v_max_f32_e32 v187, v174, v174
	v_max_f32_e32 v186, v187, v186
	v_max_f32_e32 v187, v177, v177
	v_max_f32_e32 v188, v176, v176
	v_max_f32_e32 v187, v188, v187
	s_nop 0
	v_max_f32_e32 v188, v173, v173
	v_max_f32_e32 v189, v172, v172
	v_max_f32_e32 v188, v189, v188
	v_max3_f32 v188, v170, v171, v188
	v_max3_f32 v186, v186, v187, v188
	v_max3_f32 v0, v0, v153, v186
	v_mov_b32_e32 v153, v0
	s_nop 1
	v_permlane16_swap_b32_e32 v0, v153
	v_max_f32_e32 v153, v153, v153
	v_max_f32_e32 v0, v0, v0
	v_max_f32_e32 v0, v0, v153
	v_mov_b32_e32 v153, v0
	s_nop 1
	v_permlane32_swap_b32_e32 v0, v153
	v_max_f32_e32 v153, v153, v153
	v_max_f32_e32 v0, v0, v0
	v_max_f32_e32 v0, v0, v153
	v_sub_f32_e32 v153, v0, v202
	v_mul_f32_e32 v153, 0x3e38aa3b, v153
	v_cmp_lt_f32_e32 vcc, s12, v153
	s_cbranch_vccz .LBB0_738
	v_max_f32_e32 v0, v0, v0
	v_max_f32_e32 v153, v202, v202
	v_max_f32_e32 v153, v153, v0
	v_sub_f32_e32 v0, v202, v153
	v_mul_f32_e32 v0, 0x3e38aa3b, v0
	v_exp_f32_e32 v0, v0
	v_mov_b32_e32 v202, v153
	v_pk_mul_f32 v[168:169], v[168:169], v[0:1] op_sel_hi:[1,0]
	v_pk_mul_f32 v[166:167], v[166:167], v[0:1] op_sel_hi:[1,0]
	v_pk_mul_f32 v[164:165], v[164:165], v[0:1] op_sel_hi:[1,0]
	v_pk_mul_f32 v[162:163], v[162:163], v[0:1] op_sel_hi:[1,0]
	v_pk_mul_f32 v[160:161], v[160:161], v[0:1] op_sel_hi:[1,0]
	v_pk_mul_f32 v[158:159], v[158:159], v[0:1] op_sel_hi:[1,0]
	v_pk_mul_f32 v[156:157], v[156:157], v[0:1] op_sel_hi:[1,0]
	v_pk_mul_f32 v[154:155], v[154:155], v[0:1] op_sel_hi:[1,0]
	v_mul_f32_e32 v244, v244, v0
.LBB0_738:
	v_mul_f32_e32 v187, 0xbe38aa3b, v202
	v_fmamk_f32 v0, v182, 0x3e38aa3b, v187
	v_exp_f32_e32 v0, v0
	v_fmamk_f32 v182, v183, 0x3e38aa3b, v187
	v_exp_f32_e32 v186, v182
	v_fmamk_f32 v182, v184, 0x3e38aa3b, v187
	v_exp_f32_e32 v184, v182
	v_fmamk_f32 v182, v185, 0x3e38aa3b, v187
	v_exp_f32_e32 v185, v182
	v_fmamk_f32 v178, v178, 0x3e38aa3b, v187
	v_add_f32_e32 v153, 0, v0
	v_exp_f32_e32 v178, v178
	v_fmamk_f32 v179, v179, 0x3e38aa3b, v187
	v_add_f32_e32 v153, v186, v153
	v_exp_f32_e32 v179, v179
	v_fmamk_f32 v180, v180, 0x3e38aa3b, v187
	v_add_f32_e32 v153, v184, v153
	v_exp_f32_e32 v180, v180
	v_fmamk_f32 v181, v181, 0x3e38aa3b, v187
	v_add_f32_e32 v153, v185, v153
	v_exp_f32_e32 v181, v181
	v_fmamk_f32 v174, v174, 0x3e38aa3b, v187
	v_add_f32_e32 v153, v178, v153
	v_exp_f32_e32 v188, v174
	v_fmamk_f32 v174, v175, 0x3e38aa3b, v187
	v_add_f32_e32 v153, v179, v153
	v_exp_f32_e32 v189, v174
	v_fmamk_f32 v174, v176, 0x3e38aa3b, v187
	v_add_f32_e32 v153, v180, v153
	v_exp_f32_e32 v190, v174
	v_fmamk_f32 v174, v177, 0x3e38aa3b, v187
	v_add_f32_e32 v153, v181, v153
	v_exp_f32_e32 v191, v174
	v_fmamk_f32 v170, v170, 0x3e38aa3b, v187
	v_add_f32_e32 v153, v188, v153
	v_exp_f32_e32 v192, v170
	v_fmamk_f32 v170, v171, 0x3e38aa3b, v187
	v_add_f32_e32 v153, v189, v153
	v_exp_f32_e32 v193, v170
	v_fmamk_f32 v170, v172, 0x3e38aa3b, v187
	v_add_f32_e32 v153, v190, v153
	v_exp_f32_e32 v194, v170
	v_fmamk_f32 v170, v173, 0x3e38aa3b, v187
	v_add_f32_e32 v153, v191, v153
	v_exp_f32_e32 v195, v170
	v_add_f32_e32 v153, v192, v153
	v_add_f32_e32 v153, v193, v153
	v_add_f32_e32 v153, v194, v153
	v_add_f32_e32 v153, v195, v153
	v_mov_b32_e32 v170, v153
	s_nop 1
	v_permlane16_swap_b32_e32 v153, v170
	v_add_f32_e32 v182, v153, v170
	v_mov_b32_e32 v183, v182
	s_waitcnt vmcnt(20)
	ds_write_b128 v235, v[46:49]
	ds_write_b128 v235, v[50:53] offset:1024
	ds_write_b128 v235, v[62:65] offset:2048
	ds_write_b128 v235, v[66:69] offset:3072
	v_cvt_pk_bf16_f32 v170, v0, v186
	v_cvt_pk_bf16_f32 v171, v184, v185
	v_cvt_pk_bf16_f32 v172, v178, v179
	v_cvt_pk_bf16_f32 v173, v180, v181
	ds_read_b64_tr_b16 v[174:175], v236
	ds_read_b64_tr_b16 v[176:177], v237
	s_waitcnt lgkmcnt(0)
	v_mfma_f32_16x16x32_bf16 v[166:169], v[174:177], v[170:173], v[166:169]
	ds_read_b64_tr_b16 v[174:175], v238
	ds_read_b64_tr_b16 v[176:177], v239
	v_permlane32_swap_b32_e32 v182, v183
	s_waitcnt lgkmcnt(0)
	v_mfma_f32_16x16x32_bf16 v[162:165], v[174:177], v[170:173], v[162:165]
	ds_read_b64_tr_b16 v[174:175], v240
	ds_read_b64_tr_b16 v[176:177], v241
	s_waitcnt lgkmcnt(0)
	v_mfma_f32_16x16x32_bf16 v[174:177], v[174:177], v[170:173], v[158:161]
	s_nop 2
	ds_read_b64_tr_b16 v[158:159], v242
	ds_read_b64_tr_b16 v[160:161], v243
	s_waitcnt vmcnt(16)
	ds_write_b128 v235, v[70:73]
	ds_write_b128 v235, v[74:77] offset:1024
	ds_write_b128 v235, v[78:81] offset:2048
	ds_write_b128 v235, v[82:85] offset:3072
	s_waitcnt lgkmcnt(4)
	v_mfma_f32_16x16x32_bf16 v[170:173], v[158:161], v[170:173], v[154:157]
	v_cvt_pk_bf16_f32 v178, v188, v189
	v_cvt_pk_bf16_f32 v179, v190, v191
	v_cvt_pk_bf16_f32 v180, v192, v193
	v_cvt_pk_bf16_f32 v181, v194, v195
	s_nop 2
	ds_read_b64_tr_b16 v[154:155], v236
	ds_read_b64_tr_b16 v[156:157], v237
	ds_read_b64_tr_b16 v[158:159], v238
	ds_read_b64_tr_b16 v[160:161], v239
	s_waitcnt lgkmcnt(2)
	v_mfma_f32_16x16x32_bf16 v[154:157], v[154:157], v[178:181], v[166:169]
	s_waitcnt lgkmcnt(0)
	v_mfma_f32_16x16x32_bf16 v[158:161], v[158:161], v[178:181], v[162:165]
	s_nop 2
	ds_read_b64_tr_b16 v[162:163], v240
	ds_read_b64_tr_b16 v[164:165], v241
	ds_read_b64_tr_b16 v[166:167], v242
	ds_read_b64_tr_b16 v[168:169], v243
	s_waitcnt lgkmcnt(2)
	v_mfma_f32_16x16x32_bf16 v[162:165], v[162:165], v[178:181], v[174:177]
	s_waitcnt lgkmcnt(0)
	v_mfma_f32_16x16x32_bf16 v[166:169], v[166:169], v[178:181], v[170:173]
	s_cmp_ge_u32 s47, s18
	s_cselect_b64 s[36:37], -1, 0
	s_and_b64 vcc, exec, s[36:37]
	s_cbranch_vccnz .LBB0_746
	s_lshr_b32 s35, s47, 2
	s_and_b32 s34, s47, 2
	s_add_i32 s35, s35, s44
	s_cmp_lg_u32 s34, 0
	s_cbranch_scc1 .LBB0_745
	s_add_u32 s12, s45, s35
	s_addc_u32 s13, s46, 0
	v_mov_b32_e32 v0, 0x1200
	v_mov_b32_e32 v56, v1
	v_mov_b32_e32 v57, v1
	s_mul_i32 s56, s13, 0x1200
	v_mad_u64_u32 v[14:15], s[12:13], s12, v0, v[214:215]
	v_mov_b32_e32 v54, v1
	v_mov_b32_e32 v55, v1
	v_mov_b64_e32 v[60:61], v[56:57]
	v_add_u32_e32 v15, s56, v15
	v_mov_b64_e32 v[58:59], v[54:55]
	s_and_saveexec_b64 s[12:13], s[28:29]
	s_cbranch_execz .LBB0_742
	global_load_dwordx4 v[58:61], v[14:15], off offset:512

.LBB0_760:
	s_waitcnt vmcnt(8)
	ds_write_b128 v196, v[138:141]
	ds_write_b128 v197, v[142:145] offset:1024
	ds_write_b128 v196, v[146:149] offset:2048
	ds_write_b128 v197, v[134:137] offset:3072
	ds_read_b128 v[138:141], v198
	ds_read_b128 v[142:145], v199
	ds_read_b128 v[146:149], v198 offset:2048
	ds_read_b128 v[134:137], v199 offset:2048
	ds_write_b128 v196, v[130:133]
	ds_write_b128 v197, v[126:129] offset:1024
	ds_write_b128 v196, v[122:125] offset:2048
	ds_write_b128 v197, v[118:121] offset:3072
	ds_read_b128 v[130:133], v198
	ds_read_b128 v[126:129], v199
	ds_read_b128 v[122:125], v198 offset:2048
	ds_read_b128 v[118:121], v199 offset:2048
	s_waitcnt lgkmcnt(0)
	v_mfma_f32_16x16x32_bf16 v[138:141], v[138:141], v[6:9], v[150:153]
	v_add_f32_e32 v0, v182, v183
	s_mov_b32 s12, 0x40c00000
	v_mfma_f32_16x16x32_bf16 v[130:133], v[130:133], v[6:9], v[174:177]
	s_waitcnt lgkmcnt(0)
	v_mfma_f32_16x16x32_bf16 v[122:125], v[122:125], v[6:9], v[178:181]
	v_mfma_f32_16x16x32_bf16 v[138:141], v[142:145], v[10:13], v[138:141]
	v_add_f32_e32 v142, v244, v0
	v_mfma_f32_16x16x32_bf16 v[144:147], v[146:149], v[6:9], v[170:173]
	v_mfma_f32_16x16x32_bf16 v[126:129], v[126:129], v[10:13], v[130:133]
	s_nop 4
	v_max_f32_e32 v0, v141, v141
	v_max_f32_e32 v143, v140, v140
	v_max_f32_e32 v0, v143, v0
	v_mfma_f32_16x16x32_bf16 v[118:121], v[118:121], v[10:13], v[122:125]
	v_max3_f32 v0, v138, v139, v0
	v_max_f32_e32 v130, v127, v127
	v_max_f32_e32 v131, v126, v126
	v_mfma_f32_16x16x32_bf16 v[134:137], v[134:137], v[10:13], v[144:147]
	v_max_f32_e32 v130, v131, v130
	s_nop 2
	v_max_f32_e32 v122, v121, v121
	v_max_f32_e32 v123, v120, v120
	v_max_f32_e32 v131, v129, v129
	v_max_f32_e32 v132, v128, v128
	v_max_f32_e32 v143, v137, v137
	v_max_f32_e32 v144, v136, v136
	v_max_f32_e32 v122, v123, v122
	v_max_f32_e32 v143, v144, v143
	v_max_f32_e32 v131, v132, v131
	v_max3_f32 v122, v118, v119, v122
	v_max3_f32 v143, v134, v135, v143
	v_max3_f32 v122, v130, v131, v122
	v_max3_f32 v0, v0, v143, v122
	v_mov_b32_e32 v122, v0
	s_nop 1
	v_permlane16_swap_b32_e32 v0, v122
	v_max_f32_e32 v122, v122, v122
	v_max_f32_e32 v0, v0, v0
	v_max_f32_e32 v0, v0, v122
	v_mov_b32_e32 v122, v0
	s_nop 1
	v_permlane32_swap_b32_e32 v0, v122
	v_max_f32_e32 v122, v122, v122
	v_max_f32_e32 v0, v0, v0
	v_max_f32_e32 v0, v0, v122
	v_sub_f32_e32 v122, v0, v202
	v_mul_f32_e32 v122, 0x3e38aa3b, v122
	v_cmp_lt_f32_e32 vcc, s12, v122
	s_cbranch_vccz .LBB0_762
	v_max_f32_e32 v0, v0, v0
	v_max_f32_e32 v122, v202, v202
	v_max_f32_e32 v143, v122, v0
	v_sub_f32_e32 v0, v202, v143
	v_mul_f32_e32 v0, 0x3e38aa3b, v0
	v_exp_f32_e32 v202, v0
	s_nop 0
	v_pk_mul_f32 v[186:187], v[142:143], v[202:203]
	v_pk_mul_f32 v[156:157], v[156:157], v[202:203] op_sel_hi:[1,0]
	v_pk_mul_f32 v[154:155], v[154:155], v[202:203] op_sel_hi:[1,0]
	v_pk_mul_f32 v[160:161], v[160:161], v[202:203] op_sel_hi:[1,0]
	v_pk_mul_f32 v[158:159], v[158:159], v[202:203] op_sel_hi:[1,0]
	v_pk_mul_f32 v[164:165], v[164:165], v[202:203] op_sel_hi:[1,0]
	v_pk_mul_f32 v[162:163], v[162:163], v[202:203] op_sel_hi:[1,0]
	v_pk_mul_f32 v[168:169], v[168:169], v[202:203] op_sel_hi:[1,0]
	v_pk_mul_f32 v[166:167], v[166:167], v[202:203] op_sel_hi:[1,0]
	v_mov_b32_e32 v202, v143
	v_mov_b32_e32 v142, v186
.LBB0_762:
	v_fmamk_f32 v0, v138, 0x3e38aa3b, v187
	v_exp_f32_e32 v0, v0
	v_fmamk_f32 v122, v139, 0x3e38aa3b, v187
	v_exp_f32_e32 v122, v122
	v_fmamk_f32 v123, v140, 0x3e38aa3b, v187
	v_exp_f32_e32 v123, v123
	v_fmamk_f32 v124, v141, 0x3e38aa3b, v187
	v_exp_f32_e32 v124, v124
	v_fmamk_f32 v130, v134, 0x3e38aa3b, v187
	v_add_f32_e32 v125, 0, v0
	v_exp_f32_e32 v130, v130
	v_fmamk_f32 v131, v135, 0x3e38aa3b, v187
	v_add_f32_e32 v125, v122, v125
	v_exp_f32_e32 v131, v131
	v_fmamk_f32 v132, v136, 0x3e38aa3b, v187
	v_add_f32_e32 v125, v123, v125
	v_exp_f32_e32 v132, v132
	v_fmamk_f32 v133, v137, 0x3e38aa3b, v187
	v_add_f32_e32 v125, v124, v125
	v_exp_f32_e32 v133, v133
	v_fmamk_f32 v126, v126, 0x3e38aa3b, v187
	v_add_f32_e32 v125, v130, v125
	v_exp_f32_e32 v126, v126
	v_fmamk_f32 v127, v127, 0x3e38aa3b, v187
	v_add_f32_e32 v125, v131, v125
	v_exp_f32_e32 v127, v127
	v_fmamk_f32 v128, v128, 0x3e38aa3b, v187
	v_add_f32_e32 v125, v132, v125
	v_exp_f32_e32 v128, v128
	v_fmamk_f32 v129, v129, 0x3e38aa3b, v187
	v_add_f32_e32 v125, v133, v125
	v_exp_f32_e32 v129, v129
	v_fmamk_f32 v118, v118, 0x3e38aa3b, v187
	v_add_f32_e32 v125, v126, v125
	v_exp_f32_e32 v134, v118
	v_fmamk_f32 v118, v119, 0x3e38aa3b, v187
	v_add_f32_e32 v125, v127, v125
	v_exp_f32_e32 v135, v118
	v_fmamk_f32 v118, v120, 0x3e38aa3b, v187
	v_add_f32_e32 v125, v128, v125
	v_exp_f32_e32 v136, v118
	v_fmac_f32_e32 v187, 0x3e38aa3b, v121
	v_add_f32_e32 v125, v129, v125
	v_exp_f32_e32 v137, v187
	v_add_f32_e32 v118, v134, v125
	v_add_f32_e32 v118, v135, v118
	v_add_f32_e32 v118, v136, v118
	v_add_f32_e32 v118, v137, v118
	v_mov_b32_e32 v119, v118
	s_nor_b64 s[12:13], s[26:27], s[30:31]
	s_nop 0
	v_permlane16_swap_b32_e32 v118, v119
	v_add_f32_e32 v125, v118, v119
	v_mov_b32_e32 v138, v125
	s_waitcnt vmcnt(4)
	ds_write_b128 v235, v[102:105]
	ds_write_b128 v235, v[106:109] offset:1024
	ds_write_b128 v235, v[110:113] offset:2048
	ds_write_b128 v235, v[114:117] offset:3072
	v_cvt_pk_bf16_f32 v102, v0, v122
	v_cvt_pk_bf16_f32 v103, v123, v124
	v_cvt_pk_bf16_f32 v104, v130, v131
	v_cvt_pk_bf16_f32 v105, v132, v133
	ds_read_b64_tr_b16 v[106:107], v236
	ds_read_b64_tr_b16 v[108:109], v237
	ds_read_b64_tr_b16 v[110:111], v238
	ds_read_b64_tr_b16 v[112:113], v239
	ds_read_b64_tr_b16 v[114:115], v240
	ds_read_b64_tr_b16 v[116:117], v241
	ds_read_b64_tr_b16 v[118:119], v242
	ds_read_b64_tr_b16 v[120:121], v243
	s_waitcnt vmcnt(0)
	ds_write_b128 v235, v[86:89]
	ds_write_b128 v235, v[90:93] offset:1024
	ds_write_b128 v235, v[94:97] offset:2048
	ds_write_b128 v235, v[98:101] offset:3072
	v_cvt_pk_bf16_f32 v86, v126, v127
	v_cvt_pk_bf16_f32 v87, v128, v129
	v_cvt_pk_bf16_f32 v88, v134, v135
	v_cvt_pk_bf16_f32 v89, v136, v137
	ds_read_b64_tr_b16 v[90:91], v236
	ds_read_b64_tr_b16 v[92:93], v237
	ds_read_b64_tr_b16 v[98:99], v238
	ds_read_b64_tr_b16 v[100:101], v239
	s_waitcnt lgkmcnt(14)
	v_mfma_f32_16x16x32_bf16 v[106:109], v[106:109], v[102:105], v[154:157]
	v_permlane32_swap_b32_e32 v125, v138
	v_add_f32_e32 v0, v125, v138
	s_waitcnt lgkmcnt(12)
	v_mfma_f32_16x16x32_bf16 v[110:113], v[110:113], v[102:105], v[158:161]
	v_add_f32_e32 v244, v142, v0
	s_waitcnt lgkmcnt(10)
	v_mfma_f32_16x16x32_bf16 v[114:117], v[114:117], v[102:105], v[162:165]
	s_waitcnt lgkmcnt(8)
	v_mfma_f32_16x16x32_bf16 v[94:97], v[118:121], v[102:105], v[166:169]
	s_waitcnt lgkmcnt(2)
	v_mfma_f32_16x16x32_bf16 v[166:169], v[90:93], v[86:89], v[106:109]
	ds_read_b64_tr_b16 v[90:91], v240
	ds_read_b64_tr_b16 v[92:93], v241
	s_waitcnt lgkmcnt(2)
	v_mfma_f32_16x16x32_bf16 v[162:165], v[98:101], v[86:89], v[110:113]
	ds_read_b64_tr_b16 v[98:99], v242
	ds_read_b64_tr_b16 v[100:101], v243
	s_waitcnt lgkmcnt(2)
	v_mfma_f32_16x16x32_bf16 v[158:161], v[90:93], v[86:89], v[114:117]
	s_waitcnt lgkmcnt(0)
	v_mfma_f32_16x16x32_bf16 v[154:157], v[98:101], v[86:89], v[94:97]
	s_and_saveexec_b64 s[34:35], s[12:13]
	s_xor_b64 s[12:13], exec, s[34:35]
	s_cbranch_execz .LBB0_764
	v_div_scale_f32 v0, s[34:35], v244, v244, 1.0
	v_rcp_f32_e32 v6, v0
	s_ashr_i32 s35, s42, 31
	v_div_scale_f32 v7, vcc, 1.0, v244, 1.0
	v_fma_f32 v8, -v0, v6, 1.0
	v_fmac_f32_e32 v6, v8, v6
	s_add_u32 s34, s0, s42
	v_mul_f32_e32 v8, v7, v6
	s_addc_u32 s35, s1, s35
	v_fma_f32 v9, -v0, v8, v7
	s_lshl_b64 s[34:35], s[34:35], 11
	v_fmac_f32_e32 v8, v9, v6
	s_add_u32 s34, s60, s34
	v_fma_f32 v0, -v0, v8, v7
	s_addc_u32 s35, s61, s35
	v_mov_b32_e32 v217, v1
	v_div_fmas_f32 v0, v0, v6, v8
	v_lshl_add_u64 v[6:7], s[34:35], 0, v[216:217]
	v_lshl_add_u64 v[6:7], v[210:211], 1, v[6:7]
	s_mov_b64 s[16:17], 0x13c00200
	v_div_fixup_f32 v0, v0, v244, 1.0
	v_lshl_add_u64 v[8:9], v[6:7], 0, s[16:17]
	s_mov_b32 s16, 0x13c00000
	v_mul_f32_e32 v10, v0, v166
	v_mul_f32_e32 v11, v0, v167
	v_add_co_u32_e32 v6, vcc, s16, v6
	v_cvt_pk_bf16_f32 v10, v10, v11
	v_mul_f32_e32 v11, v0, v168
	s_nop 0
	v_addc_co_u32_e32 v7, vcc, 0, v7, vcc
	v_mul_f32_e32 v12, v0, v169
	v_cvt_pk_bf16_f32 v11, v11, v12
	global_store_dwordx2 v[6:7], v[10:11], off offset:512
	v_mul_f32_e32 v6, v0, v162
	v_mul_f32_e32 v7, v0, v163
	v_cvt_pk_bf16_f32 v6, v6, v7
	v_mul_f32_e32 v7, v0, v164
	v_mul_f32_e32 v10, v0, v165
	v_cvt_pk_bf16_f32 v7, v7, v10
	global_store_dwordx2 v[8:9], v[6:7], off offset:32
	v_mul_f32_e32 v6, v0, v158
	v_mul_f32_e32 v7, v0, v159
	v_cvt_pk_bf16_f32 v6, v6, v7
	v_mul_f32_e32 v7, v0, v160
	v_mul_f32_e32 v10, v0, v161
	v_cvt_pk_bf16_f32 v7, v7, v10
	global_store_dwordx2 v[8:9], v[6:7], off offset:64
	v_mul_f32_e32 v6, v0, v154
	v_mul_f32_e32 v7, v0, v155
	v_cvt_pk_bf16_f32 v6, v6, v7
	v_mul_f32_e32 v7, v0, v156
	v_mul_f32_e32 v0, v0, v157
	v_cvt_pk_bf16_f32 v7, v7, v0
	global_store_dwordx2 v[8:9], v[6:7], off offset:96
